# speedup vs baseline: 1.0054x; 1.0011x over previous
_Z13gemm8p_kernel5GArgs:
	s_add_i32 s3, s2, 0x120
	s_sub_i32 s26, s2, 0xc0
	s_cmp_lt_u32 s2, 0xc0
	s_cselect_b32 s2, s3, s26
	s_load_dwordx4 s[20:23], s[0:1], 0x80
	s_load_dwordx8 s[4:11], s[0:1], 0x0
	s_load_dwordx8 s[12:19], s[0:1], 0x48
	s_load_dwordx2 s[24:25], s[0:1], 0x38
	v_and_b32_e32 v2, 32, v0
	s_waitcnt lgkmcnt(0)
	s_cmp_lt_i32 s2, s22
	s_cselect_b64 s[26:27], -1, 0
	s_and_b64 s[28:29], s[26:27], exec
	s_cselect_b32 s12, s4, s12
	s_cselect_b32 s3, s25, s21
	s_cselect_b32 s4, 0, s22
	s_cselect_b32 s13, s5, s13
	s_cselect_b32 s7, s7, s15
	s_cselect_b32 s14, s6, s14
	s_sub_i32 s2, s2, s4
	s_lshl_b32 s4, s3, 2
	s_lshl_b32 s3, s3, 4
	s_abs_i32 s15, s3
	v_cvt_f32_u32_e32 v1, s15
	s_ashr_i32 s5, s2, 31
	s_lshr_b32 s5, s5, 29
	s_add_i32 s5, s2, s5
	v_rcp_iflag_f32_e32 v1, v1
	s_ashr_i32 s6, s5, 3
	s_and_b32 s5, s5, -8
	s_sub_i32 s2, s2, s5
	v_mul_f32_e32 v1, 0x4f7ffffe, v1
	v_cvt_u32_f32_e32 v1, v1
	s_lshr_b32 s5, s2, 31
	s_or_b32 s4, s5, s4
	s_mul_i32 s2, s4, s2
	s_add_i32 s2, s2, s6
	s_sub_i32 s6, 0, s15
	v_readfirstlane_b32 s21, v1
	s_mul_i32 s6, s6, s21
	s_mul_hi_u32 s6, s21, s6
	s_abs_i32 s5, s2
	s_add_i32 s21, s21, s6
	s_mul_hi_u32 s6, s5, s21
	s_mul_i32 s21, s6, s15
	s_xor_b32 s4, s2, s3
	s_sub_i32 s5, s5, s21
	s_ashr_i32 s4, s4, 31
	s_add_i32 s21, s6, 1
	s_sub_i32 s22, s5, s15
	s_cmp_ge_u32 s5, s15
	s_cselect_b32 s6, s21, s6
	s_cselect_b32 s5, s22, s5
	s_add_i32 s21, s6, 1
	s_cmp_ge_u32 s5, s15
	s_cselect_b32 s5, s21, s6
	s_xor_b32 s5, s5, s4
	s_sub_i32 s4, s5, s4
	s_lshl_b32 s5, s4, 4
	s_sub_i32 s6, 32, s5
	s_min_i32 s6, s6, 16
	s_abs_i32 s15, s6
	v_cvt_f32_u32_e32 v1, s15
	s_sub_i32 s21, 0, s15
	s_mul_i32 s4, s4, s3
	s_sub_i32 s2, s2, s4
	v_rcp_iflag_f32_e32 v1, v1
	s_abs_i32 s4, s2
	s_xor_b32 s3, s2, s6
	s_ashr_i32 s3, s3, 31
	v_mul_f32_e32 v1, 0x4f7ffffe, v1
	v_cvt_u32_f32_e32 v1, v1
	v_bfe_u32 v155, v0, 2, 4
	v_mov_b32_e32 v3, 0
	v_lshrrev_b32_e32 v6, 3, v0
	v_readfirstlane_b32 s22, v1
	s_mul_i32 s21, s21, s22
	s_mul_hi_u32 s21, s22, s21
	s_add_i32 s22, s22, s21
	s_mul_hi_u32 s21, s4, s22
	s_mul_i32 s22, s21, s15
	s_sub_i32 s4, s4, s22
	s_add_i32 s22, s21, 1
	s_sub_i32 s23, s4, s15
	s_cmp_ge_u32 s4, s15
	s_cselect_b32 s21, s22, s21
	s_cselect_b32 s4, s23, s4
	s_add_i32 s22, s21, 1
	s_cmp_ge_u32 s4, s15
	s_cselect_b32 s4, s22, s21
	s_xor_b32 s4, s4, s3
	s_sub_i32 s4, s4, s3
	s_mul_i32 s3, s4, s6
	s_sub_i32 s2, s2, s3
	s_add_i32 s15, s2, s5
	s_cmp_lg_u64 s[26:27], 0
	s_cselect_b32 s5, 8, 5
	s_sub_i32 s4, s5, s4
	s_nop 0
	s_lshl_b32 s2, s4, 8
	s_lshl_b32 s6, s15, 8
	s_ashr_i32 s3, s2, 31
	v_lshlrev_b32_e32 v1, 4, v0
	s_mul_i32 s4, s4, 0x30000
	v_bitop3_b32 v2, v1, v2, 48 bitop3:0x6c
	s_mul_hi_i32 s5, s2, 0x300
	s_add_u32 s4, s14, s4
	v_and_or_b32 v2, v0, 64, v2
	s_addc_u32 s5, s7, s5
	v_or_b32_e32 v38, 0x10000, v1
	v_lshl_add_u64 v[4:5], s[4:5], 0, v[2:3]
	v_and_or_b32 v7, v6, 48, v155
	v_readfirstlane_b32 s4, v38
	v_mul_u32_u24_e32 v18, 0x300, v7
	v_mov_b32_e32 v19, v3
	s_mov_b32 m0, s4
	v_or_b32_e32 v6, 64, v6
	s_movk_i32 s4, 0x70
	v_or_b32_e32 v41, 0x12000, v1
	v_lshl_add_u64 v[14:15], v[4:5], 0, v[18:19]
	v_and_or_b32 v6, v6, s4, v155
	v_readfirstlane_b32 s4, v41
	s_mul_i32 s15, s15, 0x30000
	global_load_lds_dwordx4 v[14:15], off
	s_mov_b32 m0, s4
	s_mul_hi_i32 s5, s6, 0x300
	s_add_u32 s4, s12, s15
	v_mul_u32_u24_e32 v20, 0x300, v6
	v_mov_b32_e32 v21, v3
	s_addc_u32 s5, s13, s5
	v_lshl_add_u64 v[16:17], v[4:5], 0, v[20:21]
	v_lshl_add_u64 v[4:5], s[4:5], 0, v[2:3]
	v_readfirstlane_b32 s4, v1
	v_or_b32_e32 v37, 0x2000, v1
	global_load_lds_dwordx4 v[16:17], off
	v_lshl_add_u64 v[10:11], v[4:5], 0, v[18:19]
	s_mov_b32 m0, s4
	v_readfirstlane_b32 s4, v37
	global_load_lds_dwordx4 v[10:11], off
	s_mov_b32 m0, s4
	s_or_b32 s4, s2, 0x80
	s_mul_hi_i32 s5, s4, 0x300
	s_mulk_i32 s4, 0x300
	s_add_u32 s4, s14, s4
	s_addc_u32 s5, s7, s5
	v_or_b32_e32 v35, 0x14000, v1
	v_lshl_add_u64 v[12:13], v[4:5], 0, v[20:21]
	v_lshl_add_u64 v[4:5], s[4:5], 0, v[2:3]
	v_readfirstlane_b32 s4, v35
	v_or_b32_e32 v36, 0x16000, v1
	global_load_lds_dwordx4 v[12:13], off
	v_lshl_add_u64 v[6:7], v[4:5], 0, v[18:19]
	s_mov_b32 m0, s4
	v_readfirstlane_b32 s4, v36
	global_load_lds_dwordx4 v[6:7], off
	s_mov_b32 m0, s4
	s_or_b32 s4, s6, 0x80
	s_mul_hi_i32 s5, s4, 0x300
	s_mulk_i32 s4, 0x300
	s_add_u32 s4, s12, s4
	s_addc_u32 s5, s13, s5
	v_or_b32_e32 v39, 0x4000, v1
	v_lshl_add_u64 v[8:9], v[4:5], 0, v[20:21]
	v_lshl_add_u64 v[4:5], s[4:5], 0, v[2:3]
	v_readfirstlane_b32 s4, v39
	v_or_b32_e32 v40, 0x6000, v1
	global_load_lds_dwordx4 v[8:9], off
	v_lshl_add_u64 v[2:3], v[4:5], 0, v[18:19]
	s_mov_b32 m0, s4
	v_readfirstlane_b32 s4, v40
	global_load_lds_dwordx4 v[2:3], off
	v_lshl_add_u64 v[4:5], v[4:5], 0, v[20:21]
	s_mov_b32 m0, s4
	v_lshrrev_b32_e32 v18, 8, v0
	global_load_lds_dwordx4 v[4:5], off
	v_cmp_eq_u32_e32 vcc, 1, v18
	s_and_saveexec_b64 s[4:5], vcc
	s_cbranch_execz .LBB2_2
	s_barrier
